# baseline (speedup 1.0000x reference)
_Z9k_binsortPKjPKiPKfPKDv4_jPiS8_PfP6__half:
	s_load_dwordx4 s[80:83], s[0:1], 0x0
	s_load_dwordx8 s[72:79], s[0:1], 0x18
	s_cmpk_ge_u32 s2, 0x200
	s_cbranch_scc1 .Lk2_prio
	s_setprio 2
	s_cmpk_ge_u32 s2, 0x100
	s_cbranch_scc1 .Lk2_prio
	s_setprio 3
